# SP1 load segments: the twelve pointer-forming SALU instructions moved into the MFMA segment behind them (four behind each of its first three MFMAs), all four GEMM K-loops and peeled first K-steps
# speedup vs baseline: 1.0094x; 1.0035x over previous
.Lp1_first:
	ds_read_b128 v[184:187], v175
	ds_read_b128 v[188:191], v176
	ds_read_b128 v[192:195], v175 offset:2048
	ds_read_b128 v[196:199], v176 offset:2048
	ds_read_b128 v[200:203], v175 offset:16384
	ds_read_b128 v[204:207], v176 offset:16384
	ds_read_b128 v[208:211], v175 offset:18432
	ds_read_b128 v[212:215], v176 offset:18432
	v_lshl_add_u64 v[248:249], v[158:159], 0, s[66:67]
	s_add_i32 m0, s77, 0x8000
	ds_read_b128 v[216:219], v178
	ds_read_b128 v[220:223], v178 offset:2048
	ds_read_b128 v[224:227], v179
	ds_read_b128 v[228:231], v179 offset:2048
	ds_read_b128 v[232:235], v178 offset:4096
	ds_read_b128 v[236:239], v178 offset:6144
	ds_read_b128 v[240:243], v179 offset:4096
	ds_read_b128 v[244:247], v179 offset:6144
	global_load_lds_dwordx4 v[248:249], off
	v_lshl_add_u64 v[248:249], v[156:157], 0, s[66:67]
	s_add_i32 m0, s77, 0xa000
	s_nop 0
	global_load_lds_dwordx4 v[248:249], off
	v_lshl_add_u64 v[248:249], v[154:155], 0, s[66:67]
	s_add_i32 m0, s77, 0xc000
	s_nop 0
	global_load_lds_dwordx4 v[248:249], off
	v_lshl_add_u64 v[248:249], v[152:153], 0, s[66:67]
	s_add_i32 m0, s77, 0xe000
	s_nop 0
	global_load_lds_dwordx4 v[248:249], off
	s_waitcnt vmcnt(8)
	s_waitcnt lgkmcnt(0)
	s_barrier
	s_setprio 1
	s_waitcnt lgkmcnt(0)
	v_mfma_f32_16x16x32_bf16 v[126:129], v[184:187], v[216:219], 0
	s_add_u32 s70, s64, s66
	s_addc_u32 s71, s65, s67
	s_add_u32 s73, s70, 0x100
	s_addc_u32 vcc_lo, s71, 0
	v_mfma_f32_16x16x32_bf16 v[122:125], v[192:195], v[216:219], 0
	s_and_b64 s[70:71], s[68:69], exec
	s_cselect_b32 s71, s47, vcc_lo
	s_cselect_b32 s70, s46, s73
	s_add_u32 s73, s15, s66
	v_mfma_f32_16x16x32_bf16 v[118:121], v[184:187], v[220:223], 0
	s_addc_u32 vcc_lo, s43, s67
	s_and_b64 s[68:69], s[68:69], exec
	s_cselect_b32 s69, s45, vcc_lo
	s_cselect_b32 s68, s44, s73
	v_mfma_f32_16x16x32_bf16 v[114:117], v[192:195], v[220:223], 0
	v_mfma_f32_16x16x32_bf16 v[110:113], v[184:187], v[232:235], 0
	v_mfma_f32_16x16x32_bf16 v[106:109], v[192:195], v[232:235], 0
	v_mfma_f32_16x16x32_bf16 v[102:105], v[184:187], v[236:239], 0
	v_mfma_f32_16x16x32_bf16 v[98:101], v[192:195], v[236:239], 0
	v_mfma_f32_16x16x32_bf16 v[126:129], v[188:191], v[224:227], v[126:129]
	v_mfma_f32_16x16x32_bf16 v[122:125], v[196:199], v[224:227], v[122:125]
	v_mfma_f32_16x16x32_bf16 v[118:121], v[188:191], v[228:231], v[118:121]
	v_mfma_f32_16x16x32_bf16 v[114:117], v[196:199], v[228:231], v[114:117]
	v_mfma_f32_16x16x32_bf16 v[110:113], v[188:191], v[240:243], v[110:113]
	v_mfma_f32_16x16x32_bf16 v[106:109], v[196:199], v[240:243], v[106:109]
	v_mfma_f32_16x16x32_bf16 v[102:105], v[188:191], v[244:247], v[102:105]
	v_mfma_f32_16x16x32_bf16 v[98:101], v[196:199], v[244:247], v[98:101]
	s_setprio 0
	s_setprio 1
	v_mfma_f32_16x16x32_bf16 v[62:65], v[200:203], v[216:219], 0
	v_mfma_f32_16x16x32_bf16 v[58:61], v[208:211], v[216:219], 0
	v_mfma_f32_16x16x32_bf16 v[54:57], v[200:203], v[220:223], 0
	v_mfma_f32_16x16x32_bf16 v[50:53], v[208:211], v[220:223], 0
	v_mfma_f32_16x16x32_bf16 v[46:49], v[200:203], v[232:235], 0
	v_mfma_f32_16x16x32_bf16 v[42:45], v[208:211], v[232:235], 0
	v_mfma_f32_16x16x32_bf16 v[38:41], v[200:203], v[236:239], 0
	v_mfma_f32_16x16x32_bf16 v[34:37], v[208:211], v[236:239], 0
	v_mfma_f32_16x16x32_bf16 v[62:65], v[204:207], v[224:227], v[62:65]
	v_mfma_f32_16x16x32_bf16 v[58:61], v[212:215], v[224:227], v[58:61]
	v_mfma_f32_16x16x32_bf16 v[54:57], v[204:207], v[228:231], v[54:57]
	v_mfma_f32_16x16x32_bf16 v[50:53], v[212:215], v[228:231], v[50:53]
	v_mfma_f32_16x16x32_bf16 v[46:49], v[204:207], v[240:243], v[46:49]
	v_mfma_f32_16x16x32_bf16 v[42:45], v[212:215], v[240:243], v[42:45]
	v_mfma_f32_16x16x32_bf16 v[38:41], v[204:207], v[244:247], v[38:41]
	v_mfma_f32_16x16x32_bf16 v[34:37], v[212:215], v[244:247], v[34:37]
	s_setprio 0
	s_barrier
	s_add_i32 s73, s87, s76
	v_lshl_add_u64 v[248:249], s[68:69], 0, v[142:143]
	s_mov_b32 m0, s73
	ds_read_b128 v[216:219], v178 offset:16384
	ds_read_b128 v[220:223], v178 offset:18432
	ds_read_b128 v[224:227], v179 offset:16384
	ds_read_b128 v[228:231], v179 offset:18432
	ds_read_b128 v[232:235], v178 offset:20480
	ds_read_b128 v[236:239], v178 offset:22528
	ds_read_b128 v[240:243], v179 offset:20480
	ds_read_b128 v[244:247], v179 offset:22528
	global_load_lds_dwordx4 v[248:249], off
	s_add_i32 m0, s73, 0x2000
	s_add_u32 vcc_lo, s68, 0x80000
	v_lshl_add_u64 v[250:251], s[68:69], 0, v[144:145]
	s_addc_u32 vcc_hi, s69, 0
	s_add_i32 s73, s89, s76
	global_load_lds_dwordx4 v[250:251], off
	v_lshl_add_u64 v[252:253], vcc, 0, v[142:143]
	s_mov_b32 m0, s73
	s_nop 0
	global_load_lds_dwordx4 v[252:253], off
	v_lshl_add_u64 v[252:253], vcc, 0, v[144:145]
	s_add_i32 m0, s73, 0x2000
	s_nop 0
	global_load_lds_dwordx4 v[252:253], off
	s_waitcnt vmcnt(6)
	s_waitcnt lgkmcnt(0)
	s_barrier
	s_setprio 1
	s_waitcnt lgkmcnt(0)
	v_mfma_f32_16x16x32_bf16 v[94:97], v[184:187], v[216:219], 0
	v_mfma_f32_16x16x32_bf16 v[90:93], v[192:195], v[216:219], 0
	v_mfma_f32_16x16x32_bf16 v[86:89], v[184:187], v[220:223], 0
	v_mfma_f32_16x16x32_bf16 v[82:85], v[192:195], v[220:223], 0
	v_mfma_f32_16x16x32_bf16 v[78:81], v[184:187], v[232:235], 0
	v_mfma_f32_16x16x32_bf16 v[74:77], v[192:195], v[232:235], 0
	v_mfma_f32_16x16x32_bf16 v[70:73], v[184:187], v[236:239], 0
	v_mfma_f32_16x16x32_bf16 v[66:69], v[192:195], v[236:239], 0
	v_mfma_f32_16x16x32_bf16 v[94:97], v[188:191], v[224:227], v[94:97]
	v_mfma_f32_16x16x32_bf16 v[90:93], v[196:199], v[224:227], v[90:93]
	v_mfma_f32_16x16x32_bf16 v[86:89], v[188:191], v[228:231], v[86:89]
	v_mfma_f32_16x16x32_bf16 v[82:85], v[196:199], v[228:231], v[82:85]
	v_mfma_f32_16x16x32_bf16 v[78:81], v[188:191], v[240:243], v[78:81]
	v_mfma_f32_16x16x32_bf16 v[74:77], v[196:199], v[240:243], v[74:77]
	v_mfma_f32_16x16x32_bf16 v[70:73], v[188:191], v[244:247], v[70:73]
	v_mfma_f32_16x16x32_bf16 v[66:69], v[196:199], v[244:247], v[66:69]
	s_setprio 0
	s_setprio 1
	v_mfma_f32_16x16x32_bf16 v[30:33], v[200:203], v[216:219], 0
	v_mfma_f32_16x16x32_bf16 v[26:29], v[208:211], v[216:219], 0
	v_mfma_f32_16x16x32_bf16 v[22:25], v[200:203], v[220:223], 0
	v_mfma_f32_16x16x32_bf16 v[18:21], v[208:211], v[220:223], 0
	v_mfma_f32_16x16x32_bf16 v[14:17], v[200:203], v[232:235], 0
	v_mfma_f32_16x16x32_bf16 v[10:13], v[208:211], v[232:235], 0
	v_mfma_f32_16x16x32_bf16 v[6:9], v[200:203], v[236:239], 0
	v_mfma_f32_16x16x32_bf16 v[2:5], v[208:211], v[236:239], 0
	v_mfma_f32_16x16x32_bf16 v[30:33], v[204:207], v[224:227], v[30:33]
	v_mfma_f32_16x16x32_bf16 v[26:29], v[212:215], v[224:227], v[26:29]
	v_mfma_f32_16x16x32_bf16 v[22:25], v[204:207], v[228:231], v[22:25]
	v_mfma_f32_16x16x32_bf16 v[18:21], v[212:215], v[228:231], v[18:21]
	v_mfma_f32_16x16x32_bf16 v[14:17], v[204:207], v[240:243], v[14:17]
	v_mfma_f32_16x16x32_bf16 v[10:13], v[212:215], v[240:243], v[10:13]
	v_mfma_f32_16x16x32_bf16 v[6:9], v[204:207], v[244:247], v[6:9]
	v_mfma_f32_16x16x32_bf16 v[2:5], v[212:215], v[244:247], v[2:5]
	s_setprio 0
	s_barrier
	s_branch .Lp1_blk3

.LBB0_101:
	s_cmp_eq_u32 s66, 0
	s_cbranch_scc1 .Lp1_first
	ds_read_b128 v[184:187], v175
	ds_read_b128 v[188:191], v176
	ds_read_b128 v[192:195], v175 offset:2048
	ds_read_b128 v[196:199], v176 offset:2048
	ds_read_b128 v[200:203], v175 offset:16384
	ds_read_b128 v[204:207], v176 offset:16384
	ds_read_b128 v[208:211], v175 offset:18432
	ds_read_b128 v[212:215], v176 offset:18432
	v_lshl_add_u64 v[248:249], v[158:159], 0, s[66:67]
	s_add_i32 m0, s77, 0x8000
	ds_read_b128 v[216:219], v178
	ds_read_b128 v[220:223], v178 offset:2048
	ds_read_b128 v[224:227], v179
	ds_read_b128 v[228:231], v179 offset:2048
	ds_read_b128 v[232:235], v178 offset:4096
	ds_read_b128 v[236:239], v178 offset:6144
	ds_read_b128 v[240:243], v179 offset:4096
	ds_read_b128 v[244:247], v179 offset:6144
	global_load_lds_dwordx4 v[248:249], off
	v_lshl_add_u64 v[248:249], v[156:157], 0, s[66:67]
	s_add_i32 m0, s77, 0xa000
	s_nop 0
	global_load_lds_dwordx4 v[248:249], off
	v_lshl_add_u64 v[248:249], v[154:155], 0, s[66:67]
	s_add_i32 m0, s77, 0xc000
	s_nop 0
	global_load_lds_dwordx4 v[248:249], off
	v_lshl_add_u64 v[248:249], v[152:153], 0, s[66:67]
	s_add_i32 m0, s77, 0xe000
	s_nop 0
	global_load_lds_dwordx4 v[248:249], off
	s_waitcnt vmcnt(8)
	s_waitcnt lgkmcnt(0)
	s_barrier
	s_setprio 1
	s_waitcnt lgkmcnt(0)
	v_mfma_f32_16x16x32_bf16 v[126:129], v[184:187], v[216:219], v[126:129]
	s_add_u32 s70, s64, s66
	s_addc_u32 s71, s65, s67
	s_add_u32 s73, s70, 0x100
	s_addc_u32 vcc_lo, s71, 0
	v_mfma_f32_16x16x32_bf16 v[122:125], v[192:195], v[216:219], v[122:125]
	s_and_b64 s[70:71], s[68:69], exec
	s_cselect_b32 s71, s47, vcc_lo
	s_cselect_b32 s70, s46, s73
	s_add_u32 s73, s15, s66
	v_mfma_f32_16x16x32_bf16 v[118:121], v[184:187], v[220:223], v[118:121]
	s_addc_u32 vcc_lo, s43, s67
	s_and_b64 s[68:69], s[68:69], exec
	s_cselect_b32 s69, s45, vcc_lo
	s_cselect_b32 s68, s44, s73
	v_mfma_f32_16x16x32_bf16 v[114:117], v[192:195], v[220:223], v[114:117]
	v_mfma_f32_16x16x32_bf16 v[110:113], v[184:187], v[232:235], v[110:113]
	v_mfma_f32_16x16x32_bf16 v[106:109], v[192:195], v[232:235], v[106:109]
	v_mfma_f32_16x16x32_bf16 v[102:105], v[184:187], v[236:239], v[102:105]
	v_mfma_f32_16x16x32_bf16 v[98:101], v[192:195], v[236:239], v[98:101]
	v_mfma_f32_16x16x32_bf16 v[126:129], v[188:191], v[224:227], v[126:129]
	v_mfma_f32_16x16x32_bf16 v[122:125], v[196:199], v[224:227], v[122:125]
	v_mfma_f32_16x16x32_bf16 v[118:121], v[188:191], v[228:231], v[118:121]
	v_mfma_f32_16x16x32_bf16 v[114:117], v[196:199], v[228:231], v[114:117]
	v_mfma_f32_16x16x32_bf16 v[110:113], v[188:191], v[240:243], v[110:113]
	v_mfma_f32_16x16x32_bf16 v[106:109], v[196:199], v[240:243], v[106:109]
	v_mfma_f32_16x16x32_bf16 v[102:105], v[188:191], v[244:247], v[102:105]
	v_mfma_f32_16x16x32_bf16 v[98:101], v[196:199], v[244:247], v[98:101]
	s_setprio 0
	s_setprio 1
	v_mfma_f32_16x16x32_bf16 v[62:65], v[200:203], v[216:219], v[62:65]
	v_mfma_f32_16x16x32_bf16 v[58:61], v[208:211], v[216:219], v[58:61]
	v_mfma_f32_16x16x32_bf16 v[54:57], v[200:203], v[220:223], v[54:57]
	v_mfma_f32_16x16x32_bf16 v[50:53], v[208:211], v[220:223], v[50:53]
	v_mfma_f32_16x16x32_bf16 v[46:49], v[200:203], v[232:235], v[46:49]
	v_mfma_f32_16x16x32_bf16 v[42:45], v[208:211], v[232:235], v[42:45]
	v_mfma_f32_16x16x32_bf16 v[38:41], v[200:203], v[236:239], v[38:41]
	v_mfma_f32_16x16x32_bf16 v[34:37], v[208:211], v[236:239], v[34:37]
	v_mfma_f32_16x16x32_bf16 v[62:65], v[204:207], v[224:227], v[62:65]
	v_mfma_f32_16x16x32_bf16 v[58:61], v[212:215], v[224:227], v[58:61]
	v_mfma_f32_16x16x32_bf16 v[54:57], v[204:207], v[228:231], v[54:57]
	v_mfma_f32_16x16x32_bf16 v[50:53], v[212:215], v[228:231], v[50:53]
	v_mfma_f32_16x16x32_bf16 v[46:49], v[204:207], v[240:243], v[46:49]
	v_mfma_f32_16x16x32_bf16 v[42:45], v[212:215], v[240:243], v[42:45]
	v_mfma_f32_16x16x32_bf16 v[38:41], v[204:207], v[244:247], v[38:41]
	v_mfma_f32_16x16x32_bf16 v[34:37], v[212:215], v[244:247], v[34:37]
	s_setprio 0
	s_barrier
	s_add_i32 s73, s87, s76
	v_lshl_add_u64 v[248:249], s[68:69], 0, v[142:143]
	s_mov_b32 m0, s73
	ds_read_b128 v[216:219], v178 offset:16384
	ds_read_b128 v[220:223], v178 offset:18432
	ds_read_b128 v[224:227], v179 offset:16384
	ds_read_b128 v[228:231], v179 offset:18432
	ds_read_b128 v[232:235], v178 offset:20480
	ds_read_b128 v[236:239], v178 offset:22528
	ds_read_b128 v[240:243], v179 offset:20480
	ds_read_b128 v[244:247], v179 offset:22528
	global_load_lds_dwordx4 v[248:249], off
	s_add_i32 m0, s73, 0x2000
	s_add_u32 vcc_lo, s68, 0x80000
	v_lshl_add_u64 v[250:251], s[68:69], 0, v[144:145]
	s_addc_u32 vcc_hi, s69, 0
	s_add_i32 s73, s89, s76
	global_load_lds_dwordx4 v[250:251], off
	v_lshl_add_u64 v[252:253], vcc, 0, v[142:143]
	s_mov_b32 m0, s73
	s_nop 0
	global_load_lds_dwordx4 v[252:253], off
	v_lshl_add_u64 v[252:253], vcc, 0, v[144:145]
	s_add_i32 m0, s73, 0x2000
	s_nop 0
	global_load_lds_dwordx4 v[252:253], off
	s_waitcnt vmcnt(6)
	s_waitcnt lgkmcnt(0)
	s_barrier
	s_setprio 1
	s_waitcnt lgkmcnt(0)
	v_mfma_f32_16x16x32_bf16 v[94:97], v[184:187], v[216:219], v[94:97]
	v_mfma_f32_16x16x32_bf16 v[90:93], v[192:195], v[216:219], v[90:93]
	v_mfma_f32_16x16x32_bf16 v[86:89], v[184:187], v[220:223], v[86:89]
	v_mfma_f32_16x16x32_bf16 v[82:85], v[192:195], v[220:223], v[82:85]
	v_mfma_f32_16x16x32_bf16 v[78:81], v[184:187], v[232:235], v[78:81]
	v_mfma_f32_16x16x32_bf16 v[74:77], v[192:195], v[232:235], v[74:77]
	v_mfma_f32_16x16x32_bf16 v[70:73], v[184:187], v[236:239], v[70:73]
	v_mfma_f32_16x16x32_bf16 v[66:69], v[192:195], v[236:239], v[66:69]
	v_mfma_f32_16x16x32_bf16 v[94:97], v[188:191], v[224:227], v[94:97]
	v_mfma_f32_16x16x32_bf16 v[90:93], v[196:199], v[224:227], v[90:93]
	v_mfma_f32_16x16x32_bf16 v[86:89], v[188:191], v[228:231], v[86:89]
	v_mfma_f32_16x16x32_bf16 v[82:85], v[196:199], v[228:231], v[82:85]
	v_mfma_f32_16x16x32_bf16 v[78:81], v[188:191], v[240:243], v[78:81]
	v_mfma_f32_16x16x32_bf16 v[74:77], v[196:199], v[240:243], v[74:77]
	v_mfma_f32_16x16x32_bf16 v[70:73], v[188:191], v[244:247], v[70:73]
	v_mfma_f32_16x16x32_bf16 v[66:69], v[196:199], v[244:247], v[66:69]
	s_setprio 0
	s_setprio 1
	v_mfma_f32_16x16x32_bf16 v[30:33], v[200:203], v[216:219], v[30:33]
	v_mfma_f32_16x16x32_bf16 v[26:29], v[208:211], v[216:219], v[26:29]
	v_mfma_f32_16x16x32_bf16 v[22:25], v[200:203], v[220:223], v[22:25]
	v_mfma_f32_16x16x32_bf16 v[18:21], v[208:211], v[220:223], v[18:21]
	v_mfma_f32_16x16x32_bf16 v[14:17], v[200:203], v[232:235], v[14:17]
	v_mfma_f32_16x16x32_bf16 v[10:13], v[208:211], v[232:235], v[10:13]
	v_mfma_f32_16x16x32_bf16 v[6:9], v[200:203], v[236:239], v[6:9]
	v_mfma_f32_16x16x32_bf16 v[2:5], v[208:211], v[236:239], v[2:5]
	v_mfma_f32_16x16x32_bf16 v[30:33], v[204:207], v[224:227], v[30:33]
	v_mfma_f32_16x16x32_bf16 v[26:29], v[212:215], v[224:227], v[26:29]
	v_mfma_f32_16x16x32_bf16 v[22:25], v[204:207], v[228:231], v[22:25]
	v_mfma_f32_16x16x32_bf16 v[18:21], v[212:215], v[228:231], v[18:21]
	v_mfma_f32_16x16x32_bf16 v[14:17], v[204:207], v[240:243], v[14:17]
	v_mfma_f32_16x16x32_bf16 v[10:13], v[212:215], v[240:243], v[10:13]
	v_mfma_f32_16x16x32_bf16 v[6:9], v[204:207], v[244:247], v[6:9]
	v_mfma_f32_16x16x32_bf16 v[2:5], v[212:215], v[244:247], v[2:5]
	s_setprio 0
	s_barrier

.Lp3_first:
	ds_read_b128 v[184:187], v174
	ds_read_b128 v[188:191], v175
	ds_read_b128 v[192:195], v174 offset:2048
	ds_read_b128 v[196:199], v175 offset:2048
	ds_read_b128 v[200:203], v174 offset:16384
	ds_read_b128 v[204:207], v175 offset:16384
	ds_read_b128 v[208:211], v174 offset:18432
	ds_read_b128 v[212:215], v175 offset:18432
	v_lshl_add_u64 v[248:249], v[158:159], 0, s[28:29]
	s_add_i32 m0, s39, 0x8000
	ds_read_b128 v[216:219], v177
	ds_read_b128 v[220:223], v177 offset:2048
	ds_read_b128 v[224:227], v178
	ds_read_b128 v[228:231], v178 offset:2048
	ds_read_b128 v[232:235], v177 offset:4096
	ds_read_b128 v[236:239], v177 offset:6144
	ds_read_b128 v[240:243], v178 offset:4096
	ds_read_b128 v[244:247], v178 offset:6144
	global_load_lds_dwordx4 v[248:249], off
	v_lshl_add_u64 v[248:249], v[156:157], 0, s[28:29]
	s_add_i32 m0, s39, 0xa000
	s_nop 0
	global_load_lds_dwordx4 v[248:249], off
	v_lshl_add_u64 v[248:249], v[154:155], 0, s[28:29]
	s_add_i32 m0, s39, 0xc000
	s_nop 0
	global_load_lds_dwordx4 v[248:249], off
	v_lshl_add_u64 v[248:249], v[144:145], 0, s[28:29]
	s_add_i32 m0, s39, 0xe000
	s_nop 0
	global_load_lds_dwordx4 v[248:249], off
	s_waitcnt vmcnt(8)
	s_waitcnt lgkmcnt(0)
	s_barrier
	s_setprio 1
	s_waitcnt lgkmcnt(0)
	v_mfma_f32_16x16x32_bf16 v[126:129], v[184:187], v[216:219], 0
	s_add_u32 s34, s2, s28
	s_addc_u32 s35, s3, s29
	s_add_u32 s77, s34, 0x63000100
	s_addc_u32 s78, s35, 0
	v_mfma_f32_16x16x32_bf16 v[122:125], v[192:195], v[216:219], 0
	s_and_b64 s[34:35], s[30:31], exec
	s_cselect_b32 s35, s7, s78
	s_cselect_b32 s34, s6, s77
	s_add_u32 s77, s25, s28
	v_mfma_f32_16x16x32_bf16 v[118:121], v[184:187], v[220:223], 0
	s_addc_u32 s78, s75, s29
	s_and_b64 s[30:31], s[30:31], exec
	s_cselect_b32 s31, s27, s78
	s_cselect_b32 s30, s26, s77
	v_mfma_f32_16x16x32_bf16 v[114:117], v[192:195], v[220:223], 0
	v_mfma_f32_16x16x32_bf16 v[110:113], v[184:187], v[232:235], 0
	v_mfma_f32_16x16x32_bf16 v[102:105], v[192:195], v[232:235], 0
	v_mfma_f32_16x16x32_bf16 v[94:97], v[184:187], v[236:239], 0
	v_mfma_f32_16x16x32_bf16 v[86:89], v[192:195], v[236:239], 0
	v_mfma_f32_16x16x32_bf16 v[126:129], v[188:191], v[224:227], v[126:129]
	v_mfma_f32_16x16x32_bf16 v[122:125], v[196:199], v[224:227], v[122:125]
	v_mfma_f32_16x16x32_bf16 v[118:121], v[188:191], v[228:231], v[118:121]
	v_mfma_f32_16x16x32_bf16 v[114:117], v[196:199], v[228:231], v[114:117]
	v_mfma_f32_16x16x32_bf16 v[110:113], v[188:191], v[240:243], v[110:113]
	v_mfma_f32_16x16x32_bf16 v[102:105], v[196:199], v[240:243], v[102:105]
	v_mfma_f32_16x16x32_bf16 v[94:97], v[188:191], v[244:247], v[94:97]
	v_mfma_f32_16x16x32_bf16 v[86:89], v[196:199], v[244:247], v[86:89]
	s_setprio 0
	s_setprio 1
	v_mfma_f32_16x16x32_bf16 v[106:109], v[200:203], v[216:219], 0
	v_mfma_f32_16x16x32_bf16 v[98:101], v[208:211], v[216:219], 0
	v_mfma_f32_16x16x32_bf16 v[90:93], v[200:203], v[220:223], 0
	v_mfma_f32_16x16x32_bf16 v[82:85], v[208:211], v[220:223], 0
	v_mfma_f32_16x16x32_bf16 v[78:81], v[200:203], v[232:235], 0
	v_mfma_f32_16x16x32_bf16 v[74:77], v[208:211], v[232:235], 0
	v_mfma_f32_16x16x32_bf16 v[70:73], v[200:203], v[236:239], 0
	v_mfma_f32_16x16x32_bf16 v[66:69], v[208:211], v[236:239], 0
	v_mfma_f32_16x16x32_bf16 v[106:109], v[204:207], v[224:227], v[106:109]
	v_mfma_f32_16x16x32_bf16 v[98:101], v[212:215], v[224:227], v[98:101]
	v_mfma_f32_16x16x32_bf16 v[90:93], v[204:207], v[228:231], v[90:93]
	v_mfma_f32_16x16x32_bf16 v[82:85], v[212:215], v[228:231], v[82:85]
	v_mfma_f32_16x16x32_bf16 v[78:81], v[204:207], v[240:243], v[78:81]
	v_mfma_f32_16x16x32_bf16 v[74:77], v[212:215], v[240:243], v[74:77]
	v_mfma_f32_16x16x32_bf16 v[70:73], v[204:207], v[244:247], v[70:73]
	v_mfma_f32_16x16x32_bf16 v[66:69], v[212:215], v[244:247], v[66:69]
	s_setprio 0
	s_barrier
	s_add_i32 s77, s45, s33
	v_lshl_add_u64 v[248:249], s[30:31], 0, v[146:147]
	s_mov_b32 m0, s77
	ds_read_b128 v[216:219], v177 offset:16384
	ds_read_b128 v[220:223], v177 offset:18432
	ds_read_b128 v[224:227], v178 offset:16384
	ds_read_b128 v[228:231], v178 offset:18432
	ds_read_b128 v[232:235], v177 offset:20480
	ds_read_b128 v[236:239], v177 offset:22528
	ds_read_b128 v[240:243], v178 offset:20480
	ds_read_b128 v[244:247], v178 offset:22528
	global_load_lds_dwordx4 v[248:249], off
	s_add_i32 m0, s77, 0x2000
	s_add_u32 s78, s30, 0x80000
	v_lshl_add_u64 v[250:251], s[30:31], 0, v[148:149]
	s_addc_u32 s79, s31, 0
	s_add_i32 s77, s47, s33
	global_load_lds_dwordx4 v[250:251], off
	v_lshl_add_u64 v[252:253], s[78:79], 0, v[146:147]
	s_mov_b32 m0, s77
	s_nop 0
	global_load_lds_dwordx4 v[252:253], off
	v_lshl_add_u64 v[252:253], s[78:79], 0, v[148:149]
	s_add_i32 m0, s77, 0x2000
	s_nop 0
	global_load_lds_dwordx4 v[252:253], off
	s_waitcnt vmcnt(6)
	s_waitcnt lgkmcnt(0)
	s_barrier
	s_setprio 1
	s_waitcnt lgkmcnt(0)
	v_mfma_f32_16x16x32_bf16 v[62:65], v[184:187], v[216:219], 0
	v_mfma_f32_16x16x32_bf16 v[58:61], v[192:195], v[216:219], 0
	v_mfma_f32_16x16x32_bf16 v[50:53], v[184:187], v[220:223], 0
	v_mfma_f32_16x16x32_bf16 v[42:45], v[192:195], v[220:223], 0
	v_mfma_f32_16x16x32_bf16 v[34:37], v[184:187], v[232:235], 0
	v_mfma_f32_16x16x32_bf16 v[26:29], v[192:195], v[232:235], 0
	v_mfma_f32_16x16x32_bf16 v[18:21], v[184:187], v[236:239], 0
	v_mfma_f32_16x16x32_bf16 v[10:13], v[192:195], v[236:239], 0
	v_mfma_f32_16x16x32_bf16 v[62:65], v[188:191], v[224:227], v[62:65]
	v_mfma_f32_16x16x32_bf16 v[58:61], v[196:199], v[224:227], v[58:61]
	v_mfma_f32_16x16x32_bf16 v[50:53], v[188:191], v[228:231], v[50:53]
	v_mfma_f32_16x16x32_bf16 v[42:45], v[196:199], v[228:231], v[42:45]
	v_mfma_f32_16x16x32_bf16 v[34:37], v[188:191], v[240:243], v[34:37]
	v_mfma_f32_16x16x32_bf16 v[26:29], v[196:199], v[240:243], v[26:29]
	v_mfma_f32_16x16x32_bf16 v[18:21], v[188:191], v[244:247], v[18:21]
	v_mfma_f32_16x16x32_bf16 v[10:13], v[196:199], v[244:247], v[10:13]
	s_setprio 0
	s_setprio 1
	v_mfma_f32_16x16x32_bf16 v[54:57], v[200:203], v[216:219], 0
	v_mfma_f32_16x16x32_bf16 v[46:49], v[208:211], v[216:219], 0
	v_mfma_f32_16x16x32_bf16 v[38:41], v[200:203], v[220:223], 0
	v_mfma_f32_16x16x32_bf16 v[30:33], v[208:211], v[220:223], 0
	v_mfma_f32_16x16x32_bf16 v[22:25], v[200:203], v[232:235], 0
	v_mfma_f32_16x16x32_bf16 v[14:17], v[208:211], v[232:235], 0
	v_mfma_f32_16x16x32_bf16 v[6:9], v[200:203], v[236:239], 0
	v_mfma_f32_16x16x32_bf16 v[2:5], v[208:211], v[236:239], 0
	v_mfma_f32_16x16x32_bf16 v[54:57], v[204:207], v[224:227], v[54:57]
	v_mfma_f32_16x16x32_bf16 v[46:49], v[212:215], v[224:227], v[46:49]
	v_mfma_f32_16x16x32_bf16 v[38:41], v[204:207], v[228:231], v[38:41]
	v_mfma_f32_16x16x32_bf16 v[30:33], v[212:215], v[228:231], v[30:33]
	v_mfma_f32_16x16x32_bf16 v[22:25], v[204:207], v[240:243], v[22:25]
	v_mfma_f32_16x16x32_bf16 v[14:17], v[212:215], v[240:243], v[14:17]
	v_mfma_f32_16x16x32_bf16 v[6:9], v[204:207], v[244:247], v[6:9]
	v_mfma_f32_16x16x32_bf16 v[2:5], v[212:215], v[244:247], v[2:5]
	s_setprio 0
	s_barrier
	s_branch .Lp3_blk3

.LBB0_385:
	s_cmp_eq_u32 s28, 0
	s_cbranch_scc1 .Lp3_first
	ds_read_b128 v[184:187], v174
	ds_read_b128 v[188:191], v175
	ds_read_b128 v[192:195], v174 offset:2048
	ds_read_b128 v[196:199], v175 offset:2048
	ds_read_b128 v[200:203], v174 offset:16384
	ds_read_b128 v[204:207], v175 offset:16384
	ds_read_b128 v[208:211], v174 offset:18432
	ds_read_b128 v[212:215], v175 offset:18432
	v_lshl_add_u64 v[248:249], v[158:159], 0, s[28:29]
	s_add_i32 m0, s39, 0x8000
	ds_read_b128 v[216:219], v177
	ds_read_b128 v[220:223], v177 offset:2048
	ds_read_b128 v[224:227], v178
	ds_read_b128 v[228:231], v178 offset:2048
	ds_read_b128 v[232:235], v177 offset:4096
	ds_read_b128 v[236:239], v177 offset:6144
	ds_read_b128 v[240:243], v178 offset:4096
	ds_read_b128 v[244:247], v178 offset:6144
	global_load_lds_dwordx4 v[248:249], off
	v_lshl_add_u64 v[248:249], v[156:157], 0, s[28:29]
	s_add_i32 m0, s39, 0xa000
	s_nop 0
	global_load_lds_dwordx4 v[248:249], off
	v_lshl_add_u64 v[248:249], v[154:155], 0, s[28:29]
	s_add_i32 m0, s39, 0xc000
	s_nop 0
	global_load_lds_dwordx4 v[248:249], off
	v_lshl_add_u64 v[248:249], v[144:145], 0, s[28:29]
	s_add_i32 m0, s39, 0xe000
	s_nop 0
	global_load_lds_dwordx4 v[248:249], off
	s_waitcnt vmcnt(8)
	s_waitcnt lgkmcnt(0)
	s_barrier
	s_setprio 1
	s_waitcnt lgkmcnt(0)
	v_mfma_f32_16x16x32_bf16 v[126:129], v[184:187], v[216:219], v[126:129]
	s_add_u32 s34, s2, s28
	s_addc_u32 s35, s3, s29
	s_add_u32 s77, s34, 0x63000100
	s_addc_u32 s78, s35, 0
	v_mfma_f32_16x16x32_bf16 v[122:125], v[192:195], v[216:219], v[122:125]
	s_and_b64 s[34:35], s[30:31], exec
	s_cselect_b32 s35, s7, s78
	s_cselect_b32 s34, s6, s77
	s_add_u32 s77, s25, s28
	v_mfma_f32_16x16x32_bf16 v[118:121], v[184:187], v[220:223], v[118:121]
	s_addc_u32 s78, s75, s29
	s_and_b64 s[30:31], s[30:31], exec
	s_cselect_b32 s31, s27, s78
	s_cselect_b32 s30, s26, s77
	v_mfma_f32_16x16x32_bf16 v[114:117], v[192:195], v[220:223], v[114:117]
	v_mfma_f32_16x16x32_bf16 v[110:113], v[184:187], v[232:235], v[110:113]
	v_mfma_f32_16x16x32_bf16 v[102:105], v[192:195], v[232:235], v[102:105]
	v_mfma_f32_16x16x32_bf16 v[94:97], v[184:187], v[236:239], v[94:97]
	v_mfma_f32_16x16x32_bf16 v[86:89], v[192:195], v[236:239], v[86:89]
	v_mfma_f32_16x16x32_bf16 v[126:129], v[188:191], v[224:227], v[126:129]
	v_mfma_f32_16x16x32_bf16 v[122:125], v[196:199], v[224:227], v[122:125]
	v_mfma_f32_16x16x32_bf16 v[118:121], v[188:191], v[228:231], v[118:121]
	v_mfma_f32_16x16x32_bf16 v[114:117], v[196:199], v[228:231], v[114:117]
	v_mfma_f32_16x16x32_bf16 v[110:113], v[188:191], v[240:243], v[110:113]
	v_mfma_f32_16x16x32_bf16 v[102:105], v[196:199], v[240:243], v[102:105]
	v_mfma_f32_16x16x32_bf16 v[94:97], v[188:191], v[244:247], v[94:97]
	v_mfma_f32_16x16x32_bf16 v[86:89], v[196:199], v[244:247], v[86:89]
	s_setprio 0
	s_setprio 1
	v_mfma_f32_16x16x32_bf16 v[106:109], v[200:203], v[216:219], v[106:109]
	v_mfma_f32_16x16x32_bf16 v[98:101], v[208:211], v[216:219], v[98:101]
	v_mfma_f32_16x16x32_bf16 v[90:93], v[200:203], v[220:223], v[90:93]
	v_mfma_f32_16x16x32_bf16 v[82:85], v[208:211], v[220:223], v[82:85]
	v_mfma_f32_16x16x32_bf16 v[78:81], v[200:203], v[232:235], v[78:81]
	v_mfma_f32_16x16x32_bf16 v[74:77], v[208:211], v[232:235], v[74:77]
	v_mfma_f32_16x16x32_bf16 v[70:73], v[200:203], v[236:239], v[70:73]
	v_mfma_f32_16x16x32_bf16 v[66:69], v[208:211], v[236:239], v[66:69]
	v_mfma_f32_16x16x32_bf16 v[106:109], v[204:207], v[224:227], v[106:109]
	v_mfma_f32_16x16x32_bf16 v[98:101], v[212:215], v[224:227], v[98:101]
	v_mfma_f32_16x16x32_bf16 v[90:93], v[204:207], v[228:231], v[90:93]
	v_mfma_f32_16x16x32_bf16 v[82:85], v[212:215], v[228:231], v[82:85]
	v_mfma_f32_16x16x32_bf16 v[78:81], v[204:207], v[240:243], v[78:81]
	v_mfma_f32_16x16x32_bf16 v[74:77], v[212:215], v[240:243], v[74:77]
	v_mfma_f32_16x16x32_bf16 v[70:73], v[204:207], v[244:247], v[70:73]
	v_mfma_f32_16x16x32_bf16 v[66:69], v[212:215], v[244:247], v[66:69]
	s_setprio 0
	s_barrier
	s_add_i32 s77, s45, s33
	v_lshl_add_u64 v[248:249], s[30:31], 0, v[146:147]
	s_mov_b32 m0, s77
	ds_read_b128 v[216:219], v177 offset:16384
	ds_read_b128 v[220:223], v177 offset:18432
	ds_read_b128 v[224:227], v178 offset:16384
	ds_read_b128 v[228:231], v178 offset:18432
	ds_read_b128 v[232:235], v177 offset:20480
	ds_read_b128 v[236:239], v177 offset:22528
	ds_read_b128 v[240:243], v178 offset:20480
	ds_read_b128 v[244:247], v178 offset:22528
	global_load_lds_dwordx4 v[248:249], off
	s_add_i32 m0, s77, 0x2000
	s_add_u32 s78, s30, 0x80000
	v_lshl_add_u64 v[250:251], s[30:31], 0, v[148:149]
	s_addc_u32 s79, s31, 0
	s_add_i32 s77, s47, s33
	global_load_lds_dwordx4 v[250:251], off
	v_lshl_add_u64 v[252:253], s[78:79], 0, v[146:147]
	s_mov_b32 m0, s77
	s_nop 0
	global_load_lds_dwordx4 v[252:253], off
	v_lshl_add_u64 v[252:253], s[78:79], 0, v[148:149]
	s_add_i32 m0, s77, 0x2000
	s_nop 0
	global_load_lds_dwordx4 v[252:253], off
	s_waitcnt vmcnt(6)
	s_waitcnt lgkmcnt(0)
	s_barrier
	s_setprio 1
	s_waitcnt lgkmcnt(0)
	v_mfma_f32_16x16x32_bf16 v[62:65], v[184:187], v[216:219], v[62:65]
	v_mfma_f32_16x16x32_bf16 v[58:61], v[192:195], v[216:219], v[58:61]
	v_mfma_f32_16x16x32_bf16 v[50:53], v[184:187], v[220:223], v[50:53]
	v_mfma_f32_16x16x32_bf16 v[42:45], v[192:195], v[220:223], v[42:45]
	v_mfma_f32_16x16x32_bf16 v[34:37], v[184:187], v[232:235], v[34:37]
	v_mfma_f32_16x16x32_bf16 v[26:29], v[192:195], v[232:235], v[26:29]
	v_mfma_f32_16x16x32_bf16 v[18:21], v[184:187], v[236:239], v[18:21]
	v_mfma_f32_16x16x32_bf16 v[10:13], v[192:195], v[236:239], v[10:13]
	v_mfma_f32_16x16x32_bf16 v[62:65], v[188:191], v[224:227], v[62:65]
	v_mfma_f32_16x16x32_bf16 v[58:61], v[196:199], v[224:227], v[58:61]
	v_mfma_f32_16x16x32_bf16 v[50:53], v[188:191], v[228:231], v[50:53]
	v_mfma_f32_16x16x32_bf16 v[42:45], v[196:199], v[228:231], v[42:45]
	v_mfma_f32_16x16x32_bf16 v[34:37], v[188:191], v[240:243], v[34:37]
	v_mfma_f32_16x16x32_bf16 v[26:29], v[196:199], v[240:243], v[26:29]
	v_mfma_f32_16x16x32_bf16 v[18:21], v[188:191], v[244:247], v[18:21]
	v_mfma_f32_16x16x32_bf16 v[10:13], v[196:199], v[244:247], v[10:13]
	s_setprio 0
	s_setprio 1
	v_mfma_f32_16x16x32_bf16 v[54:57], v[200:203], v[216:219], v[54:57]
	v_mfma_f32_16x16x32_bf16 v[46:49], v[208:211], v[216:219], v[46:49]
	v_mfma_f32_16x16x32_bf16 v[38:41], v[200:203], v[220:223], v[38:41]
	v_mfma_f32_16x16x32_bf16 v[30:33], v[208:211], v[220:223], v[30:33]
	v_mfma_f32_16x16x32_bf16 v[22:25], v[200:203], v[232:235], v[22:25]
	v_mfma_f32_16x16x32_bf16 v[14:17], v[208:211], v[232:235], v[14:17]
	v_mfma_f32_16x16x32_bf16 v[6:9], v[200:203], v[236:239], v[6:9]
	v_mfma_f32_16x16x32_bf16 v[2:5], v[208:211], v[236:239], v[2:5]
	v_mfma_f32_16x16x32_bf16 v[54:57], v[204:207], v[224:227], v[54:57]
	v_mfma_f32_16x16x32_bf16 v[46:49], v[212:215], v[224:227], v[46:49]
	v_mfma_f32_16x16x32_bf16 v[38:41], v[204:207], v[228:231], v[38:41]
	v_mfma_f32_16x16x32_bf16 v[30:33], v[212:215], v[228:231], v[30:33]
	v_mfma_f32_16x16x32_bf16 v[22:25], v[204:207], v[240:243], v[22:25]
	v_mfma_f32_16x16x32_bf16 v[14:17], v[212:215], v[240:243], v[14:17]
	v_mfma_f32_16x16x32_bf16 v[6:9], v[204:207], v[244:247], v[6:9]
	v_mfma_f32_16x16x32_bf16 v[2:5], v[212:215], v[244:247], v[2:5]
	s_setprio 0
	s_barrier

.Lp6_first:
	ds_read_b128 v[18:21], v208
	ds_read_b128 v[22:25], v209
	ds_read_b128 v[26:29], v208 offset:2048
	ds_read_b128 v[30:33], v209 offset:2048
	ds_read_b128 v[2:5], v208 offset:16384
	ds_read_b128 v[6:9], v209 offset:16384
	ds_read_b128 v[10:13], v208 offset:18432
	ds_read_b128 v[14:17], v209 offset:18432
	v_lshl_add_u64 v[200:201], v[190:191], 0, s[40:41]
	s_add_i32 m0, s35, 0x8000
	ds_read_b128 v[218:221], v211
	ds_read_b128 v[226:229], v211 offset:2048
	ds_read_b128 v[222:225], v212
	ds_read_b128 v[230:233], v212 offset:2048
	ds_read_b128 v[234:237], v211 offset:4096
	ds_read_b128 v[242:245], v211 offset:6144
	ds_read_b128 v[238:241], v212 offset:4096
	ds_read_b128 v[246:249], v212 offset:6144
	global_load_lds_dwordx4 v[200:201], off
	v_lshl_add_u64 v[200:201], v[188:189], 0, s[40:41]
	s_add_i32 m0, s35, 0xa000
	s_nop 0
	global_load_lds_dwordx4 v[200:201], off
	v_lshl_add_u64 v[200:201], v[186:187], 0, s[40:41]
	s_add_i32 m0, s35, 0xc000
	s_nop 0
	global_load_lds_dwordx4 v[200:201], off
	v_lshl_add_u64 v[200:201], v[184:185], 0, s[40:41]
	s_add_i32 m0, s35, 0xe000
	s_nop 0
	global_load_lds_dwordx4 v[200:201], off
	s_waitcnt vmcnt(8)
	s_waitcnt lgkmcnt(0)
	s_barrier
	s_setprio 1
	s_waitcnt lgkmcnt(0)
	v_mfma_f32_16x16x128_f8f6f4 v[158:161], v[18:25], v[218:225], 0
	s_add_u32 s44, s2, s40
	s_addc_u32 s45, s3, s41
	s_add_u32 s84, s44, 0x56800100
	s_addc_u32 s85, s45, 0
	v_mfma_f32_16x16x128_f8f6f4 v[154:157], v[26:33], v[218:225], 0
	s_and_b64 s[44:45], s[42:43], exec
	s_cselect_b32 s45, s9, s85
	s_cselect_b32 s44, s8, s84
	s_add_u32 s84, s29, s40
	v_mfma_f32_16x16x128_f8f6f4 v[150:153], v[18:25], v[226:233], 0
	s_addc_u32 s85, s37, s41
	s_and_b64 s[42:43], s[42:43], exec
	s_cselect_b32 s43, s31, s85
	s_cselect_b32 s42, s30, s84
	v_mfma_f32_16x16x128_f8f6f4 v[146:149], v[26:33], v[226:233], 0
	v_mfma_f32_16x16x128_f8f6f4 v[126:129], v[18:25], v[234:241], 0
	v_mfma_f32_16x16x128_f8f6f4 v[122:125], v[26:33], v[234:241], 0
	v_mfma_f32_16x16x128_f8f6f4 v[110:113], v[18:25], v[242:249], 0
	v_mfma_f32_16x16x128_f8f6f4 v[106:109], v[26:33], v[242:249], 0
	s_setprio 0
	s_setprio 1
	v_mfma_f32_16x16x128_f8f6f4 v[142:145], v[2:9], v[218:225], 0
	v_mfma_f32_16x16x128_f8f6f4 v[138:141], v[10:17], v[218:225], 0
	v_mfma_f32_16x16x128_f8f6f4 v[134:137], v[2:9], v[226:233], 0
	v_mfma_f32_16x16x128_f8f6f4 v[130:133], v[10:17], v[226:233], 0
	v_mfma_f32_16x16x128_f8f6f4 v[118:121], v[2:9], v[234:241], 0
	v_mfma_f32_16x16x128_f8f6f4 v[114:117], v[10:17], v[234:241], 0
	v_mfma_f32_16x16x128_f8f6f4 v[102:105], v[2:9], v[242:249], 0
	v_mfma_f32_16x16x128_f8f6f4 v[98:101], v[10:17], v[242:249], 0
	s_setprio 0
	s_barrier
	s_add_i32 s84, s68, s33
	v_lshl_add_u64 v[200:201], s[42:43], 0, v[164:165]
	s_mov_b32 m0, s84
	ds_read_b128 v[218:221], v211 offset:16384
	ds_read_b128 v[226:229], v211 offset:18432
	ds_read_b128 v[222:225], v212 offset:16384
	ds_read_b128 v[230:233], v212 offset:18432
	ds_read_b128 v[234:237], v211 offset:20480
	ds_read_b128 v[242:245], v211 offset:22528
	ds_read_b128 v[238:241], v212 offset:20480
	ds_read_b128 v[246:249], v212 offset:22528
	global_load_lds_dwordx4 v[200:201], off
	s_add_i32 m0, s84, 0x2000
	s_add_u32 s84, s42, 0x40000
	v_lshl_add_u64 v[202:203], s[42:43], 0, v[166:167]
	s_addc_u32 s85, s43, 0
	s_add_i32 s86, s70, s33
	global_load_lds_dwordx4 v[202:203], off
	v_lshl_add_u64 v[250:251], s[84:85], 0, v[164:165]
	s_mov_b32 m0, s86
	s_nop 0
	global_load_lds_dwordx4 v[250:251], off
	v_lshl_add_u64 v[250:251], s[84:85], 0, v[166:167]
	s_add_i32 m0, s86, 0x2000
	s_nop 0
	global_load_lds_dwordx4 v[250:251], off
	s_waitcnt vmcnt(6)
	s_waitcnt lgkmcnt(0)
	s_barrier
	s_setprio 1
	s_waitcnt lgkmcnt(0)
	v_mfma_f32_16x16x128_f8f6f4 v[94:97], v[18:25], v[218:225], 0
	v_mfma_f32_16x16x128_f8f6f4 v[90:93], v[26:33], v[218:225], 0
	v_mfma_f32_16x16x128_f8f6f4 v[78:81], v[18:25], v[226:233], 0
	v_mfma_f32_16x16x128_f8f6f4 v[74:77], v[26:33], v[226:233], 0
	v_mfma_f32_16x16x128_f8f6f4 v[62:65], v[18:25], v[234:241], 0
	v_mfma_f32_16x16x128_f8f6f4 v[58:61], v[26:33], v[234:241], 0
	v_mfma_f32_16x16x128_f8f6f4 v[46:49], v[18:25], v[242:249], 0
	v_mfma_f32_16x16x128_f8f6f4 v[42:45], v[26:33], v[242:249], 0
	s_setprio 0
	s_setprio 1
	v_mfma_f32_16x16x128_f8f6f4 v[86:89], v[2:9], v[218:225], 0
	v_mfma_f32_16x16x128_f8f6f4 v[82:85], v[10:17], v[218:225], 0
	v_mfma_f32_16x16x128_f8f6f4 v[70:73], v[2:9], v[226:233], 0
	v_mfma_f32_16x16x128_f8f6f4 v[66:69], v[10:17], v[226:233], 0
	v_mfma_f32_16x16x128_f8f6f4 v[54:57], v[2:9], v[234:241], 0
	v_mfma_f32_16x16x128_f8f6f4 v[50:53], v[10:17], v[234:241], 0
	v_mfma_f32_16x16x128_f8f6f4 v[38:41], v[2:9], v[242:249], 0
	v_mfma_f32_16x16x128_f8f6f4 v[34:37], v[10:17], v[242:249], 0
	s_setprio 0
	s_barrier
	s_branch .Lp6_blk3

.LBB0_777:
	s_cmp_eq_u32 s40, 0
	s_cbranch_scc1 .Lp6_first
	ds_read_b128 v[18:21], v208
	ds_read_b128 v[22:25], v209
	ds_read_b128 v[26:29], v208 offset:2048
	ds_read_b128 v[30:33], v209 offset:2048
	ds_read_b128 v[2:5], v208 offset:16384
	ds_read_b128 v[6:9], v209 offset:16384
	ds_read_b128 v[10:13], v208 offset:18432
	ds_read_b128 v[14:17], v209 offset:18432
	v_lshl_add_u64 v[200:201], v[190:191], 0, s[40:41]
	s_add_i32 m0, s35, 0x8000
	ds_read_b128 v[218:221], v211
	ds_read_b128 v[226:229], v211 offset:2048
	ds_read_b128 v[222:225], v212
	ds_read_b128 v[230:233], v212 offset:2048
	ds_read_b128 v[234:237], v211 offset:4096
	ds_read_b128 v[242:245], v211 offset:6144
	ds_read_b128 v[238:241], v212 offset:4096
	ds_read_b128 v[246:249], v212 offset:6144
	global_load_lds_dwordx4 v[200:201], off
	v_lshl_add_u64 v[200:201], v[188:189], 0, s[40:41]
	s_add_i32 m0, s35, 0xa000
	s_nop 0
	global_load_lds_dwordx4 v[200:201], off
	v_lshl_add_u64 v[200:201], v[186:187], 0, s[40:41]
	s_add_i32 m0, s35, 0xc000
	s_nop 0
	global_load_lds_dwordx4 v[200:201], off
	v_lshl_add_u64 v[200:201], v[184:185], 0, s[40:41]
	s_add_i32 m0, s35, 0xe000
	s_nop 0
	global_load_lds_dwordx4 v[200:201], off
	s_waitcnt vmcnt(8)
	s_waitcnt lgkmcnt(0)
	s_barrier
	s_setprio 1
	s_waitcnt lgkmcnt(0)
	v_mfma_f32_16x16x128_f8f6f4 v[158:161], v[18:25], v[218:225], v[158:161]
	s_add_u32 s44, s2, s40
	s_addc_u32 s45, s3, s41
	s_add_u32 s84, s44, 0x56800100
	s_addc_u32 s85, s45, 0
	v_mfma_f32_16x16x128_f8f6f4 v[154:157], v[26:33], v[218:225], v[154:157]
	s_and_b64 s[44:45], s[42:43], exec
	s_cselect_b32 s45, s9, s85
	s_cselect_b32 s44, s8, s84
	s_add_u32 s84, s29, s40
	v_mfma_f32_16x16x128_f8f6f4 v[150:153], v[18:25], v[226:233], v[150:153]
	s_addc_u32 s85, s37, s41
	s_and_b64 s[42:43], s[42:43], exec
	s_cselect_b32 s43, s31, s85
	s_cselect_b32 s42, s30, s84
	v_mfma_f32_16x16x128_f8f6f4 v[146:149], v[26:33], v[226:233], v[146:149]
	v_mfma_f32_16x16x128_f8f6f4 v[126:129], v[18:25], v[234:241], v[126:129]
	v_mfma_f32_16x16x128_f8f6f4 v[122:125], v[26:33], v[234:241], v[122:125]
	v_mfma_f32_16x16x128_f8f6f4 v[110:113], v[18:25], v[242:249], v[110:113]
	v_mfma_f32_16x16x128_f8f6f4 v[106:109], v[26:33], v[242:249], v[106:109]
	s_setprio 0
	s_setprio 1
	v_mfma_f32_16x16x128_f8f6f4 v[142:145], v[2:9], v[218:225], v[142:145]
	v_mfma_f32_16x16x128_f8f6f4 v[138:141], v[10:17], v[218:225], v[138:141]
	v_mfma_f32_16x16x128_f8f6f4 v[134:137], v[2:9], v[226:233], v[134:137]
	v_mfma_f32_16x16x128_f8f6f4 v[130:133], v[10:17], v[226:233], v[130:133]
	v_mfma_f32_16x16x128_f8f6f4 v[118:121], v[2:9], v[234:241], v[118:121]
	v_mfma_f32_16x16x128_f8f6f4 v[114:117], v[10:17], v[234:241], v[114:117]
	v_mfma_f32_16x16x128_f8f6f4 v[102:105], v[2:9], v[242:249], v[102:105]
	v_mfma_f32_16x16x128_f8f6f4 v[98:101], v[10:17], v[242:249], v[98:101]
	s_setprio 0
	s_barrier
	s_add_i32 s84, s68, s33
	v_lshl_add_u64 v[200:201], s[42:43], 0, v[164:165]
	s_mov_b32 m0, s84
	ds_read_b128 v[218:221], v211 offset:16384
	ds_read_b128 v[226:229], v211 offset:18432
	ds_read_b128 v[222:225], v212 offset:16384
	ds_read_b128 v[230:233], v212 offset:18432
	ds_read_b128 v[234:237], v211 offset:20480
	ds_read_b128 v[242:245], v211 offset:22528
	ds_read_b128 v[238:241], v212 offset:20480
	ds_read_b128 v[246:249], v212 offset:22528
	global_load_lds_dwordx4 v[200:201], off
	s_add_i32 m0, s84, 0x2000
	s_add_u32 s84, s42, 0x40000
	v_lshl_add_u64 v[202:203], s[42:43], 0, v[166:167]
	s_addc_u32 s85, s43, 0
	s_add_i32 s86, s70, s33
	global_load_lds_dwordx4 v[202:203], off
	v_lshl_add_u64 v[250:251], s[84:85], 0, v[164:165]
	s_mov_b32 m0, s86
	s_nop 0
	global_load_lds_dwordx4 v[250:251], off
	v_lshl_add_u64 v[250:251], s[84:85], 0, v[166:167]
	s_add_i32 m0, s86, 0x2000
	s_nop 0
	global_load_lds_dwordx4 v[250:251], off
	s_waitcnt vmcnt(6)
	s_waitcnt lgkmcnt(0)
	s_barrier
	s_setprio 1
	s_waitcnt lgkmcnt(0)
	v_mfma_f32_16x16x128_f8f6f4 v[94:97], v[18:25], v[218:225], v[94:97]
	v_mfma_f32_16x16x128_f8f6f4 v[90:93], v[26:33], v[218:225], v[90:93]
	v_mfma_f32_16x16x128_f8f6f4 v[78:81], v[18:25], v[226:233], v[78:81]
	v_mfma_f32_16x16x128_f8f6f4 v[74:77], v[26:33], v[226:233], v[74:77]
	v_mfma_f32_16x16x128_f8f6f4 v[62:65], v[18:25], v[234:241], v[62:65]
	v_mfma_f32_16x16x128_f8f6f4 v[58:61], v[26:33], v[234:241], v[58:61]
	v_mfma_f32_16x16x128_f8f6f4 v[46:49], v[18:25], v[242:249], v[46:49]
	v_mfma_f32_16x16x128_f8f6f4 v[42:45], v[26:33], v[242:249], v[42:45]
	s_setprio 0
	s_setprio 1
	v_mfma_f32_16x16x128_f8f6f4 v[86:89], v[2:9], v[218:225], v[86:89]
	v_mfma_f32_16x16x128_f8f6f4 v[82:85], v[10:17], v[218:225], v[82:85]
	v_mfma_f32_16x16x128_f8f6f4 v[70:73], v[2:9], v[226:233], v[70:73]
	v_mfma_f32_16x16x128_f8f6f4 v[66:69], v[10:17], v[226:233], v[66:69]
	v_mfma_f32_16x16x128_f8f6f4 v[54:57], v[2:9], v[234:241], v[54:57]
	v_mfma_f32_16x16x128_f8f6f4 v[50:53], v[10:17], v[234:241], v[50:53]
	v_mfma_f32_16x16x128_f8f6f4 v[38:41], v[2:9], v[242:249], v[38:41]
	v_mfma_f32_16x16x128_f8f6f4 v[34:37], v[10:17], v[242:249], v[34:37]
	s_setprio 0
	s_barrier

.Lp7_first:
	ds_read_b128 v[18:21], v210
	ds_read_b128 v[22:25], v211
	ds_read_b128 v[26:29], v210 offset:2048
	ds_read_b128 v[30:33], v211 offset:2048
	ds_read_b128 v[2:5], v210 offset:16384
	ds_read_b128 v[6:9], v211 offset:16384
	ds_read_b128 v[10:13], v210 offset:18432
	ds_read_b128 v[14:17], v211 offset:18432
	v_lshl_add_u64 v[200:201], v[190:191], 0, s[44:45]
	s_add_i32 m0, s41, 0x8000
	ds_read_b128 v[220:223], v213
	ds_read_b128 v[228:231], v213 offset:2048
	ds_read_b128 v[224:227], v214
	ds_read_b128 v[232:235], v214 offset:2048
	ds_read_b128 v[236:239], v213 offset:4096
	ds_read_b128 v[244:247], v213 offset:6144
	ds_read_b128 v[240:243], v214 offset:4096
	ds_read_b128 v[248:251], v214 offset:6144
	global_load_lds_dwordx4 v[200:201], off
	v_lshl_add_u64 v[200:201], v[188:189], 0, s[44:45]
	s_add_i32 m0, s41, 0xa000
	s_nop 0
	global_load_lds_dwordx4 v[200:201], off
	v_lshl_add_u64 v[200:201], v[186:187], 0, s[44:45]
	s_add_i32 m0, s41, 0xc000
	s_nop 0
	global_load_lds_dwordx4 v[200:201], off
	v_lshl_add_u64 v[200:201], v[184:185], 0, s[44:45]
	s_add_i32 m0, s41, 0xe000
	s_nop 0
	global_load_lds_dwordx4 v[200:201], off
	s_waitcnt vmcnt(8)
	s_waitcnt lgkmcnt(0)
	s_barrier
	s_setprio 1
	s_waitcnt lgkmcnt(0)
	v_mfma_f32_16x16x128_f8f6f4 v[158:161], v[18:25], v[220:227], 0
	s_add_u32 s48, s2, s44
	s_addc_u32 s49, s3, s45
	s_add_u32 s81, s48, 0x3e800100
	s_addc_u32 s82, s49, 0
	v_mfma_f32_16x16x128_f8f6f4 v[154:157], v[26:33], v[220:227], 0
	s_and_b64 s[48:49], s[46:47], exec
	s_cselect_b32 s49, s9, s82
	s_cselect_b32 s48, s8, s81
	s_add_u32 s81, s35, s44
	v_mfma_f32_16x16x128_f8f6f4 v[150:153], v[18:25], v[228:235], 0
	s_addc_u32 s82, s37, s45
	s_and_b64 s[46:47], s[46:47], exec
	s_cselect_b32 s47, s39, s82
	s_cselect_b32 s46, s38, s81
	v_mfma_f32_16x16x128_f8f6f4 v[146:149], v[26:33], v[228:235], 0
	v_mfma_f32_16x16x128_f8f6f4 v[142:145], v[18:25], v[236:243], 0
	v_mfma_f32_16x16x128_f8f6f4 v[138:141], v[26:33], v[236:243], 0
	v_mfma_f32_16x16x128_f8f6f4 v[134:137], v[18:25], v[244:251], 0
	v_mfma_f32_16x16x128_f8f6f4 v[130:133], v[26:33], v[244:251], 0
	s_setprio 0
	s_setprio 1
	v_mfma_f32_16x16x128_f8f6f4 v[102:105], v[2:9], v[220:227], 0
	v_mfma_f32_16x16x128_f8f6f4 v[94:97], v[10:17], v[220:227], 0
	v_mfma_f32_16x16x128_f8f6f4 v[86:89], v[2:9], v[228:235], 0
	v_mfma_f32_16x16x128_f8f6f4 v[82:85], v[10:17], v[228:235], 0
	v_mfma_f32_16x16x128_f8f6f4 v[78:81], v[2:9], v[236:243], 0
	v_mfma_f32_16x16x128_f8f6f4 v[74:77], v[10:17], v[236:243], 0
	v_mfma_f32_16x16x128_f8f6f4 v[70:73], v[2:9], v[244:251], 0
	v_mfma_f32_16x16x128_f8f6f4 v[66:69], v[10:17], v[244:251], 0
	s_setprio 0
	s_barrier
	s_add_i32 s81, s66, s51
	v_lshl_add_u64 v[200:201], s[46:47], 0, v[162:163]
	s_mov_b32 m0, s81
	ds_read_b128 v[220:223], v213 offset:16384
	ds_read_b128 v[228:231], v213 offset:18432
	ds_read_b128 v[224:227], v214 offset:16384
	ds_read_b128 v[232:235], v214 offset:18432
	ds_read_b128 v[236:239], v213 offset:20480
	ds_read_b128 v[244:247], v213 offset:22528
	ds_read_b128 v[240:243], v214 offset:20480
	ds_read_b128 v[248:251], v214 offset:22528
	global_load_lds_dwordx4 v[200:201], off
	s_add_i32 m0, s81, 0x2000
	s_add_u32 s82, s46, 0x40000
	v_lshl_add_u64 v[202:203], s[46:47], 0, v[164:165]
	s_addc_u32 s83, s47, 0
	s_add_i32 s81, s68, s51
	global_load_lds_dwordx4 v[202:203], off
	v_lshl_add_u64 v[252:253], s[82:83], 0, v[162:163]
	s_mov_b32 m0, s81
	s_nop 0
	global_load_lds_dwordx4 v[252:253], off
	v_lshl_add_u64 v[252:253], s[82:83], 0, v[164:165]
	s_add_i32 m0, s81, 0x2000
	s_nop 0
	global_load_lds_dwordx4 v[252:253], off
	s_waitcnt vmcnt(6)
	s_waitcnt lgkmcnt(0)
	s_barrier
	s_setprio 1
	s_waitcnt lgkmcnt(0)
	v_mfma_f32_16x16x128_f8f6f4 v[126:129], v[18:25], v[220:227], 0
	v_mfma_f32_16x16x128_f8f6f4 v[122:125], v[26:33], v[220:227], 0
	v_mfma_f32_16x16x128_f8f6f4 v[118:121], v[18:25], v[228:235], 0
	v_mfma_f32_16x16x128_f8f6f4 v[114:117], v[26:33], v[228:235], 0
	v_mfma_f32_16x16x128_f8f6f4 v[110:113], v[18:25], v[236:243], 0
	v_mfma_f32_16x16x128_f8f6f4 v[106:109], v[26:33], v[236:243], 0
	v_mfma_f32_16x16x128_f8f6f4 v[98:101], v[18:25], v[244:251], 0
	v_mfma_f32_16x16x128_f8f6f4 v[90:93], v[26:33], v[244:251], 0
	s_setprio 0
	s_setprio 1
	v_mfma_f32_16x16x128_f8f6f4 v[62:65], v[2:9], v[220:227], 0
	v_mfma_f32_16x16x128_f8f6f4 v[58:61], v[10:17], v[220:227], 0
	v_mfma_f32_16x16x128_f8f6f4 v[54:57], v[2:9], v[228:235], 0
	v_mfma_f32_16x16x128_f8f6f4 v[50:53], v[10:17], v[228:235], 0
	v_mfma_f32_16x16x128_f8f6f4 v[46:49], v[2:9], v[236:243], 0
	v_mfma_f32_16x16x128_f8f6f4 v[42:45], v[10:17], v[236:243], 0
	v_mfma_f32_16x16x128_f8f6f4 v[38:41], v[2:9], v[244:251], 0
	v_mfma_f32_16x16x128_f8f6f4 v[34:37], v[10:17], v[244:251], 0
	s_setprio 0
	s_barrier
	s_branch .Lp7_blk3

.LBB0_862:
	s_cmp_eq_u32 s44, 0
	s_cbranch_scc1 .Lp7_first
	ds_read_b128 v[18:21], v210
	ds_read_b128 v[22:25], v211
	ds_read_b128 v[26:29], v210 offset:2048
	ds_read_b128 v[30:33], v211 offset:2048
	ds_read_b128 v[2:5], v210 offset:16384
	ds_read_b128 v[6:9], v211 offset:16384
	ds_read_b128 v[10:13], v210 offset:18432
	ds_read_b128 v[14:17], v211 offset:18432
	v_lshl_add_u64 v[200:201], v[190:191], 0, s[44:45]
	s_add_i32 m0, s41, 0x8000
	ds_read_b128 v[220:223], v213
	ds_read_b128 v[228:231], v213 offset:2048
	ds_read_b128 v[224:227], v214
	ds_read_b128 v[232:235], v214 offset:2048
	ds_read_b128 v[236:239], v213 offset:4096
	ds_read_b128 v[244:247], v213 offset:6144
	ds_read_b128 v[240:243], v214 offset:4096
	ds_read_b128 v[248:251], v214 offset:6144
	global_load_lds_dwordx4 v[200:201], off
	v_lshl_add_u64 v[200:201], v[188:189], 0, s[44:45]
	s_add_i32 m0, s41, 0xa000
	s_nop 0
	global_load_lds_dwordx4 v[200:201], off
	v_lshl_add_u64 v[200:201], v[186:187], 0, s[44:45]
	s_add_i32 m0, s41, 0xc000
	s_nop 0
	global_load_lds_dwordx4 v[200:201], off
	v_lshl_add_u64 v[200:201], v[184:185], 0, s[44:45]
	s_add_i32 m0, s41, 0xe000
	s_nop 0
	global_load_lds_dwordx4 v[200:201], off
	s_waitcnt vmcnt(8)
	s_waitcnt lgkmcnt(0)
	s_barrier
	s_setprio 1
	s_waitcnt lgkmcnt(0)
	v_mfma_f32_16x16x128_f8f6f4 v[158:161], v[18:25], v[220:227], v[158:161]
	s_add_u32 s48, s2, s44
	s_addc_u32 s49, s3, s45
	s_add_u32 s81, s48, 0x3e800100
	s_addc_u32 s82, s49, 0
	v_mfma_f32_16x16x128_f8f6f4 v[154:157], v[26:33], v[220:227], v[154:157]
	s_and_b64 s[48:49], s[46:47], exec
	s_cselect_b32 s49, s9, s82
	s_cselect_b32 s48, s8, s81
	s_add_u32 s81, s35, s44
	v_mfma_f32_16x16x128_f8f6f4 v[150:153], v[18:25], v[228:235], v[150:153]
	s_addc_u32 s82, s37, s45
	s_and_b64 s[46:47], s[46:47], exec
	s_cselect_b32 s47, s39, s82
	s_cselect_b32 s46, s38, s81
	v_mfma_f32_16x16x128_f8f6f4 v[146:149], v[26:33], v[228:235], v[146:149]
	v_mfma_f32_16x16x128_f8f6f4 v[142:145], v[18:25], v[236:243], v[142:145]
	v_mfma_f32_16x16x128_f8f6f4 v[138:141], v[26:33], v[236:243], v[138:141]
	v_mfma_f32_16x16x128_f8f6f4 v[134:137], v[18:25], v[244:251], v[134:137]
	v_mfma_f32_16x16x128_f8f6f4 v[130:133], v[26:33], v[244:251], v[130:133]
	s_setprio 0
	s_setprio 1
	v_mfma_f32_16x16x128_f8f6f4 v[102:105], v[2:9], v[220:227], v[102:105]
	v_mfma_f32_16x16x128_f8f6f4 v[94:97], v[10:17], v[220:227], v[94:97]
	v_mfma_f32_16x16x128_f8f6f4 v[86:89], v[2:9], v[228:235], v[86:89]
	v_mfma_f32_16x16x128_f8f6f4 v[82:85], v[10:17], v[228:235], v[82:85]
	v_mfma_f32_16x16x128_f8f6f4 v[78:81], v[2:9], v[236:243], v[78:81]
	v_mfma_f32_16x16x128_f8f6f4 v[74:77], v[10:17], v[236:243], v[74:77]
	v_mfma_f32_16x16x128_f8f6f4 v[70:73], v[2:9], v[244:251], v[70:73]
	v_mfma_f32_16x16x128_f8f6f4 v[66:69], v[10:17], v[244:251], v[66:69]
	s_setprio 0
	s_barrier
	s_add_i32 s81, s66, s51
	v_lshl_add_u64 v[200:201], s[46:47], 0, v[162:163]
	s_mov_b32 m0, s81
	ds_read_b128 v[220:223], v213 offset:16384
	ds_read_b128 v[228:231], v213 offset:18432
	ds_read_b128 v[224:227], v214 offset:16384
	ds_read_b128 v[232:235], v214 offset:18432
	ds_read_b128 v[236:239], v213 offset:20480
	ds_read_b128 v[244:247], v213 offset:22528
	ds_read_b128 v[240:243], v214 offset:20480
	ds_read_b128 v[248:251], v214 offset:22528
	global_load_lds_dwordx4 v[200:201], off
	s_add_i32 m0, s81, 0x2000
	s_add_u32 s82, s46, 0x40000
	v_lshl_add_u64 v[202:203], s[46:47], 0, v[164:165]
	s_addc_u32 s83, s47, 0
	s_add_i32 s81, s68, s51
	global_load_lds_dwordx4 v[202:203], off
	v_lshl_add_u64 v[252:253], s[82:83], 0, v[162:163]
	s_mov_b32 m0, s81
	s_nop 0
	global_load_lds_dwordx4 v[252:253], off
	v_lshl_add_u64 v[252:253], s[82:83], 0, v[164:165]
	s_add_i32 m0, s81, 0x2000
	s_nop 0
	global_load_lds_dwordx4 v[252:253], off
	s_waitcnt vmcnt(6)
	s_waitcnt lgkmcnt(0)
	s_barrier
	s_setprio 1
	s_waitcnt lgkmcnt(0)
	v_mfma_f32_16x16x128_f8f6f4 v[126:129], v[18:25], v[220:227], v[126:129]
	v_mfma_f32_16x16x128_f8f6f4 v[122:125], v[26:33], v[220:227], v[122:125]
	v_mfma_f32_16x16x128_f8f6f4 v[118:121], v[18:25], v[228:235], v[118:121]
	v_mfma_f32_16x16x128_f8f6f4 v[114:117], v[26:33], v[228:235], v[114:117]
	v_mfma_f32_16x16x128_f8f6f4 v[110:113], v[18:25], v[236:243], v[110:113]
	v_mfma_f32_16x16x128_f8f6f4 v[106:109], v[26:33], v[236:243], v[106:109]
	v_mfma_f32_16x16x128_f8f6f4 v[98:101], v[18:25], v[244:251], v[98:101]
	v_mfma_f32_16x16x128_f8f6f4 v[90:93], v[26:33], v[244:251], v[90:93]
	s_setprio 0
	s_setprio 1
	v_mfma_f32_16x16x128_f8f6f4 v[62:65], v[2:9], v[220:227], v[62:65]
	v_mfma_f32_16x16x128_f8f6f4 v[58:61], v[10:17], v[220:227], v[58:61]
	v_mfma_f32_16x16x128_f8f6f4 v[54:57], v[2:9], v[228:235], v[54:57]
	v_mfma_f32_16x16x128_f8f6f4 v[50:53], v[10:17], v[228:235], v[50:53]
	v_mfma_f32_16x16x128_f8f6f4 v[46:49], v[2:9], v[236:243], v[46:49]
	v_mfma_f32_16x16x128_f8f6f4 v[42:45], v[10:17], v[236:243], v[42:45]
	v_mfma_f32_16x16x128_f8f6f4 v[38:41], v[2:9], v[244:251], v[38:41]
	v_mfma_f32_16x16x128_f8f6f4 v[34:37], v[10:17], v[244:251], v[34:37]
	s_setprio 0
	s_barrier
